# dsaq projection GEMM moved to the start of the prep phase so the dynamic queues absorb its 2-vs-1 tile imbalance
# speedup vs baseline: 1.0136x; 1.0012x over previous
_Z10fwd_kernel6Params:
	s_mov_b32 s100, 0
	v_writelane_b32 v255, s100, 7
	s_mov_b32 s100, 0
	v_writelane_b32 v255, s100, 9
	s_mov_b32 s88, s2
	s_load_dword s2, s[0:1], 0xc0
	v_cmp_gt_u32_e32 vcc, 16, v0
	s_waitcnt lgkmcnt(0)
	v_writelane_b32 v252, s2, 0
	s_add_u32 s2, s0, 0xc0
	s_addc_u32 s3, s1, 0
	v_writelane_b32 v252, s2, 1
	s_nop 1
	v_writelane_b32 v252, s3, 2
	s_and_saveexec_b64 s[2:3], vcc
	v_lshl_add_u32 v1, v0, 2, 0
	v_add_u32_e32 v1, 0x21000, v1
	v_mov_b32_e32 v2, 0
	ds_write_b32 v1, v2
	s_or_b64 exec, exec, s[2:3]
	s_load_dwordx4 s[84:87], s[0:1], 0xa8
	v_cmp_gt_u32_e32 vcc, 21, v0
	s_and_saveexec_b64 s[2:3], vcc
	s_cbranch_execz .LBB0_4
	v_lshlrev_b32_e32 v1, 3, v0
	global_load_dwordx2 v[2:3], v1, s[0:1]
	v_add_u32_e32 v1, 0, v1
	v_add_u32_e32 v1, 0x21040, v1
	s_waitcnt vmcnt(0)
	ds_write_b64 v1, v[2:3]
